# exp1_skip_own_poll
# speedup vs baseline: 1.0178x; 1.0178x over previous
.LBB1_88:
	s_or_b64 exec, exec, s[26:27]
	v_mov_b32_e32 v2, v0
	s_waitcnt lgkmcnt(0)
	s_barrier
	s_lshl_b32 s30, s36, 1
	v_ashrrev_i32_e32 v3, 5, v2
	v_lshlrev_b32_e32 v2, 4, v2
	v_and_b32_e32 v2, 0x1f0, v2
	v_min_i32_e32 v4, 0x53, v3
	v_lshl_or_b32 v4, v4, 9, v2
	v_min_i32_e32 v5, 0x43, v3
	v_lshl_or_b32 v5, v5, 9, v2
	ds_read_b128 v[54:57], v4
	ds_read_b128 v[50:53], v5 offset:8192
	v_min_i32_e32 v4, 51, v3
	v_lshl_or_b32 v4, v4, 9, v2
	v_min_i32_e32 v5, 35, v3
	v_lshl_or_b32 v5, v5, 9, v2
	ds_read_b128 v[46:49], v4 offset:16384
	ds_read_b128 v[42:45], v5 offset:24576
	v_min_i32_e32 v4, 19, v3
	v_lshl_or_b32 v4, v4, 9, v2
	v_min_i32_e32 v3, 3, v3
	v_lshl_or_b32 v2, v3, 9, v2
	ds_read_b128 v[38:41], v4 offset:32768
	ds_read_b128 v[34:37], v2 offset:40960
	s_lshl_b64 s[26:27], s[36:37], 17
	v_lshl_add_u64 v[2:3], v[212:213], 0, s[26:27]
	v_add_co_u32_e32 v4, vcc, s65, v2
	global_load_dwordx4 v[100:103], v[2:3], off
	global_load_dwordx4 v[92:95], v[2:3], off offset:1024
	global_load_dwordx4 v[88:91], v[2:3], off offset:2048
	global_load_dwordx4 v[80:83], v[2:3], off offset:3072
	v_addc_co_u32_e32 v5, vcc, 0, v3, vcc
	v_add_co_u32_e32 v6, vcc, s75, v2
	s_lshl_b32 s26, s36, 9
	s_nop 0
	v_addc_co_u32_e32 v7, vcc, 0, v3, vcc
	v_add_co_u32_e32 v2, vcc, s66, v2
	s_mov_b32 s27, s37
	s_nop 0
	v_addc_co_u32_e32 v3, vcc, 0, v3, vcc
	v_lshl_add_u64 v[14:15], s[26:27], 2, v[218:219]
	global_load_dwordx4 v[84:87], v[4:5], off offset:1024
	global_load_dwordx4 v[76:79], v[4:5], off offset:2048
	global_load_dwordx4 v[96:99], v[6:7], off offset:-4096
	global_load_dwordx4 v[128:131], v[6:7], off
	global_load_dwordx4 v[124:127], v[6:7], off offset:1024
	global_load_dwordx4 v[120:123], v[6:7], off offset:2048
	global_load_dwordx4 v[112:115], v[6:7], off offset:3072
	global_load_dwordx4 v[68:71], v[4:5], off offset:3072
	global_load_dwordx4 v[116:119], v[2:3], off
	global_load_dwordx4 v[108:111], v[2:3], off offset:1024
	global_load_dwordx4 v[104:107], v[2:3], off offset:2048
	global_load_dwordx4 v[72:75], v[2:3], off offset:3072
	global_load_dwordx4 v[18:21], v[14:15], off offset:1536
	global_load_dwordx4 v[22:25], v[14:15], off offset:1568
	s_nop 0
	global_load_dwordx4 v[2:5], v[14:15], off offset:1664
	global_load_dwordx4 v[6:9], v[14:15], off offset:1696
	global_load_dwordx4 v[26:29], v[14:15], off offset:1600
	global_load_dwordx4 v[30:33], v[14:15], off offset:1632
	global_load_dwordx4 v[10:13], v[14:15], off offset:1728
	s_nop 0
	global_load_dwordx4 v[14:17], v[14:15], off offset:1760
	v_mov_b32_e32 v58, v0
	s_or_b32 s80, s30, 1
	s_lshl_b32 s26, s36, 7
	s_nop 0
	v_cmp_gt_i32_e32 vcc, s76, v58
	s_and_saveexec_b64 s[30:31], vcc
	s_cbranch_execz .LBB1_126
	s_lshl_b32 s81, s80, 5
	s_lshl_b64 s[40:41], s[26:27], 2
	s_add_u32 s40, s22, s40
	s_addc_u32 s41, s23, s41
	v_ashrrev_i32_e32 v59, 31, v58
	v_lshl_add_u64 v[60:61], v[58:59], 2, s[40:41]
	global_load_dword v59, v[60:61], off
	v_and_b32_e32 v60, 63, v58
	v_cmp_gt_u32_e32 vcc, 32, v60
	s_and_saveexec_b64 s[40:41], vcc
	s_cbranch_execz .LBB1_125
	v_lshlrev_b32_e32 v60, 8, v60
	v_mov_b32_e32 v61, v66
	v_lshl_add_u64 v[60:61], s[34:35], 0, v[60:61]
	s_mov_b32 s82, 0x10000
	s_mov_b64 s[42:43], 0
	s_branch .LBB1_114

.LBB1_169:
	s_or_b64 exec, exec, s[30:31]
	v_mov_b32_e32 v2, v0
	s_waitcnt lgkmcnt(0)
	s_barrier
	s_nop 0
	v_ashrrev_i32_e32 v3, 5, v2
	v_lshlrev_b32_e32 v2, 4, v2
	v_and_b32_e32 v2, 0x1f0, v2
	v_min_i32_e32 v4, 0x53, v3
	v_lshl_or_b32 v4, v4, 9, v2
	v_min_i32_e32 v5, 0x43, v3
	v_lshl_or_b32 v5, v5, 9, v2
	ds_read_b128 v[42:45], v4
	ds_read_b128 v[38:41], v5 offset:8192
	v_min_i32_e32 v4, 51, v3
	v_lshl_or_b32 v4, v4, 9, v2
	v_min_i32_e32 v5, 35, v3
	v_lshl_or_b32 v5, v5, 9, v2
	ds_read_b128 v[34:37], v4 offset:16384
	ds_read_b128 v[30:33], v5 offset:24576
	v_min_i32_e32 v4, 19, v3
	v_lshl_or_b32 v4, v4, 9, v2
	v_min_i32_e32 v3, 3, v3
	v_lshl_or_b32 v2, v3, 9, v2
	ds_read_b128 v[22:25], v4 offset:32768
	ds_read_b128 v[18:21], v2 offset:40960
	s_add_i32 s80, s36, 1
	s_cmp_lg_u32 s36, 2
	s_cselect_b64 s[30:31], -1, 0
	s_and_b64 s[40:41], s[30:31], exec
	s_cselect_b32 s42, s80, 2
	s_lshl_b32 s40, s42, 15
	s_mov_b32 s41, s37
	v_lshl_add_u64 v[2:3], v[196:197], 0, s[40:41]
	v_lshl_add_u64 v[4:5], v[198:199], 0, s[40:41]
	v_lshl_add_u64 v[6:7], v[200:201], 0, s[40:41]
	global_load_dwordx4 v[116:119], v[2:3], off
	global_load_dwordx4 v[120:123], v[2:3], off offset:1024
	global_load_dwordx4 v[112:115], v[4:5], off
	global_load_dwordx4 v[100:103], v[4:5], off offset:1024
	global_load_dwordx4 v[96:99], v[6:7], off
	global_load_dwordx4 v[76:79], v[6:7], off offset:1024
	global_load_dwordx4 v[124:127], v[2:3], off offset:2048
	global_load_dwordx4 v[128:131], v[2:3], off offset:3072
	global_load_dwordx4 v[104:107], v[4:5], off offset:2048
	global_load_dwordx4 v[108:111], v[4:5], off offset:3072
	global_load_dwordx4 v[72:75], v[6:7], off offset:2048
	global_load_dwordx4 v[68:71], v[6:7], off offset:3072
	v_add_co_u32_e32 v2, vcc, s65, v2
	s_lshl_b32 s40, s42, 7
	s_nop 0
	v_addc_co_u32_e32 v3, vcc, 0, v3, vcc
	v_add_co_u32_e32 v4, vcc, s65, v4
	v_lshl_add_u64 v[14:15], s[40:41], 2, v[202:203]
	s_nop 0
	v_addc_co_u32_e32 v5, vcc, 0, v5, vcc
	v_add_co_u32_e32 v6, vcc, s65, v6
	s_nop 1
	v_addc_co_u32_e32 v7, vcc, 0, v7, vcc
	global_load_dwordx4 v[148:151], v[2:3], off
	global_load_dwordx4 v[152:155], v[2:3], off offset:1024
	global_load_dwordx4 v[132:135], v[4:5], off
	global_load_dwordx4 v[136:139], v[4:5], off offset:1024
	global_load_dwordx4 v[92:95], v[6:7], off
	global_load_dwordx4 v[84:87], v[6:7], off offset:1024
	global_load_dwordx4 v[156:159], v[2:3], off offset:2048
	global_load_dwordx4 v[160:163], v[2:3], off offset:3072
	global_load_dwordx4 v[140:143], v[4:5], off offset:2048
	global_load_dwordx4 v[144:147], v[4:5], off offset:3072
	global_load_dwordx4 v[88:91], v[6:7], off offset:2048
	global_load_dwordx4 v[80:83], v[6:7], off offset:3072
	s_nop 0
	global_load_dwordx4 v[2:5], v[14:15], off
	global_load_dwordx4 v[6:9], v[14:15], off offset:32
	global_load_dwordx4 v[10:13], v[14:15], off offset:64
	s_nop 0
	global_load_dwordx4 v[14:17], v[14:15], off offset:96
	s_nop 0
	global_load_dwordx4 v[26:29], v[216:217], off offset:1024
	v_mov_b32_e32 v46, v0
	s_nop 0
	v_cmp_gt_i32_e32 vcc, s76, v46
	s_and_saveexec_b64 s[40:41], vcc
	s_cbranch_execz .LBB1_207
	s_lshl_b32 s36, s36, 6
	s_add_i32 s36, s36, 64
	s_lshl_b64 s[26:27], s[26:27], 2
	s_add_u32 s26, s24, s26
	s_addc_u32 s27, s25, s27
	v_ashrrev_i32_e32 v47, 31, v46
	v_lshl_add_u64 v[48:49], v[46:47], 2, s[26:27]
	global_load_dword v47, v[48:49], off
	v_and_b32_e32 v48, 63, v46
	v_cmp_gt_u32_e32 vcc, 32, v48
	s_and_saveexec_b64 s[26:27], vcc
	s_cbranch_execz .LBB1_206
	v_lshlrev_b32_e32 v48, 8, v48
	v_mov_b32_e32 v49, v66
	v_lshl_add_u64 v[48:49], s[34:35], 0, v[48:49]
	s_mov_b32 s81, 0x10000
	s_mov_b64 s[42:43], 0
	s_branch .LBB1_195
